# speedup vs baseline: 1.0434x; 1.0434x over previous
_Z16sum_layer_kernelPKfS0_Pf:
	s_load_dwordx4 s[4:7], s[0:1], 0x0
	s_load_dwordx2 s[8:9], s[0:1], 0x10
	v_lshrrev_b32_e32 v42, 6, v0
	v_bfe_u32 v41, v0, 5, 1
	v_and_b32_e32 v40, 31, v0
	v_readfirstlane_b32 s23, v42
	v_and_b32_e32 v43, 7, v0
	v_bfe_u32 v44, v0, 3, 3
	s_lshl_b32 s3, s2, 12
	s_lshl_b32 s19, s2, 7
	s_lshl_b32 s23, s23, 12
	v_lshlrev_b32_e32 v1, 11, v41
	v_lshl_or_b32 v1, v40, 2, v1
	s_mov_b32 m0, s23
	v_lshrrev_b32_e32 v46, 1, v44
	v_xor_b32_e32 v46, v43, v46
	v_lshlrev_b32_e32 v46, 4, v46
	v_lshl_add_u32 v35, v44, 16, v46
	v_lshl_add_u32 v35, v42, 21, v35
	v_add_u32_e32 v35, s19, v35
	v_xor_b32_e32 v86, 64, v35
	s_mov_b32 s20, 0x7fc00
	s_mov_b32 s21, 0xff800
	s_mov_b32 s22, 0x17f400
	s_mov_b32 s14, 0x200000
	s_mov_b32 s15, 0x20000
	v_and_b32_e32 v45, 63, v0
	v_lshlrev_b32_e32 v37, 4, v45
	s_add_u32 s54, s23, 0x4000
	s_waitcnt lgkmcnt(0)
	s_mov_b32 s12, s6
	s_and_b32 s13, s7, 0xffff
	s_and_b32 s5, s5, 0xffff
	s_mov_b32 s6, 0x800000
	s_mov_b32 s7, s15
	s_mov_b32 m0, s54
	s_nop 0
	buffer_load_dwordx4 v37, s[12:15], s3 offen nt lds
	buffer_load_dwordx4 v37, s[12:15], s3 offen offset:1024 nt lds
	buffer_load_dwordx4 v37, s[12:15], s3 offen offset:2048 nt lds
	buffer_load_dwordx4 v37, s[12:15], s3 offen offset:3072 nt lds
	s_mov_b32 m0, s23
	s_nop 0
	buffer_load_dwordx4 v35, s[4:7], 0 offen nt lds
	buffer_load_dwordx4 v86, s[4:7], s20 offen offset:1024 nt lds
	buffer_load_dwordx4 v35, s[4:7], s21 offen offset:2048 nt lds
	buffer_load_dwordx4 v86, s[4:7], s22 offen offset:3072 nt lds
	v_and_b32_e32 v45, 63, v0
	v_lshlrev_b32_e32 v36, 2, v40
	v_lshl_add_u32 v36, v41, 18, v36
	v_lshl_add_u32 v36, v42, 21, v36
	v_add_u32_e32 v36, s19, v36
	v_bfe_u32 v47, v40, 1, 3
	v_lshlrev_b32_e32 v39, 2, v41
	v_xor_b32_e32 v39, v39, v47
	v_lshlrev_b32_e32 v39, 4, v39
	v_lshl_add_u32 v39, v40, 7, v39
	v_lshl_add_u32 v39, v42, 12, v39
	v_xor_b32_e32 v81, 16, v39
	v_xor_b32_e32 v82, 32, v39
	v_xor_b32_e32 v83, 48, v39
	v_cmp_gt_u32_e32 vcc, 32, v45
	v_mov_b32_e32 v34, 0xc1600000
	v_mov_b32_e32 v84, 0x3fb8aa3b
	v_mov_b32_e32 v85, 0x3f317218
	s_lshl_b32 s24, 1, 16
	s_lshl_b32 s25, 2, 16
	s_lshl_b32 s26, 3, 16
	s_lshl_b32 s27, 8, 16
	s_lshl_b32 s28, 9, 16
	s_lshl_b32 s29, 10, 16
	s_lshl_b32 s30, 11, 16
	s_lshl_b32 s31, 16, 16
	s_lshl_b32 s32, 17, 16
	s_lshl_b32 s33, 18, 16
	s_lshl_b32 s34, 19, 16
	s_lshl_b32 s35, 24, 16
	s_lshl_b32 s36, 25, 16
	s_lshl_b32 s37, 26, 16
	s_lshl_b32 s38, 27, 16
	s_and_b32 s9, s9, 0xffff
	s_mov_b32 s10, s6
	s_mov_b32 s11, s15
	v_lshl_add_u32 v38, v42, 12, v1
	v_add_u32_e32 v38, 0x4000, v38
	v_add_u32_e32 v87, 0x400, v38
	s_waitcnt vmcnt(4)
	ds_read2_b32 v[18:19], v38 offset0:0 offset1:32
	ds_read2_b32 v[20:21], v38 offset0:64 offset1:96
	ds_read2_b32 v[22:23], v38 offset0:128 offset1:160
	ds_read2_b32 v[24:25], v38 offset0:192 offset1:224
	ds_read2_b32 v[26:27], v87 offset0:0 offset1:32
	ds_read2_b32 v[28:29], v87 offset0:64 offset1:96
	ds_read2_b32 v[30:31], v87 offset0:128 offset1:160
	ds_read2_b32 v[32:33], v87 offset0:192 offset1:224
	s_waitcnt lgkmcnt(0)
	v_max3_f32 v48, v18, v19, v20
	v_max3_f32 v50, v21, v22, v23
	v_max3_f32 v48, v48, v24, v25
	v_max3_f32 v50, v50, v26, v27
	v_max3_f32 v48, v48, v28, v29
	v_max3_f32 v50, v50, v30, v31
	v_max3_f32 v48, v48, v32, v33
	v_max_f32_e32 v48, v48, v50
	v_mov_b32_e32 v50, v48
	s_nop 1
	v_permlane32_swap_b32_e32 v48, v50
	v_max_f32_e32 v48, v48, v50
	v_fmamk_f32 v48, v48, 0x3fb8aa3b, v34
	v_pk_fma_f32 v[18:19], v[18:19], v[84:85], v[48:49] op_sel_hi:[1,0,0] neg_lo:[0,0,1] neg_hi:[0,0,1]
	v_exp_f32_e32 v18, v18
	v_exp_f32_e32 v19, v19
	v_pk_fma_f32 v[20:21], v[20:21], v[84:85], v[48:49] op_sel_hi:[1,0,0] neg_lo:[0,0,1] neg_hi:[0,0,1]
	v_exp_f32_e32 v20, v20
	v_exp_f32_e32 v21, v21
	v_pk_fma_f32 v[22:23], v[22:23], v[84:85], v[48:49] op_sel_hi:[1,0,0] neg_lo:[0,0,1] neg_hi:[0,0,1]
	v_exp_f32_e32 v22, v22
	v_exp_f32_e32 v23, v23
	v_pk_fma_f32 v[24:25], v[24:25], v[84:85], v[48:49] op_sel_hi:[1,0,0] neg_lo:[0,0,1] neg_hi:[0,0,1]
	v_exp_f32_e32 v24, v24
	v_exp_f32_e32 v25, v25
	v_pk_fma_f32 v[26:27], v[26:27], v[84:85], v[48:49] op_sel_hi:[1,0,0] neg_lo:[0,0,1] neg_hi:[0,0,1]
	v_exp_f32_e32 v26, v26
	v_exp_f32_e32 v27, v27
	v_pk_fma_f32 v[28:29], v[28:29], v[84:85], v[48:49] op_sel_hi:[1,0,0] neg_lo:[0,0,1] neg_hi:[0,0,1]
	v_exp_f32_e32 v28, v28
	v_exp_f32_e32 v29, v29
	v_pk_fma_f32 v[30:31], v[30:31], v[84:85], v[48:49] op_sel_hi:[1,0,0] neg_lo:[0,0,1] neg_hi:[0,0,1]
	v_exp_f32_e32 v30, v30
	v_exp_f32_e32 v31, v31
	v_pk_fma_f32 v[32:33], v[32:33], v[84:85], v[48:49] op_sel_hi:[1,0,0] neg_lo:[0,0,1] neg_hi:[0,0,1]
	v_exp_f32_e32 v32, v32
	v_exp_f32_e32 v33, v33
	v_pk_add_f32 v[56:57], v[18:19], v[20:21]
	v_pk_add_f32 v[58:59], v[22:23], v[24:25]
	v_pk_add_f32 v[60:61], v[26:27], v[28:29]
	v_pk_add_f32 v[62:63], v[30:31], v[32:33]
	v_pk_add_f32 v[56:57], v[56:57], v[58:59]
	v_pk_add_f32 v[60:61], v[60:61], v[62:63]
	v_pk_add_f32 v[56:57], v[56:57], v[60:61]
	v_add_f32_e32 v50, v56, v57
	v_mov_b32_e32 v51, v50
	s_nop 1
	v_permlane32_swap_b32_e32 v50, v51
	v_add_f32_e32 v50, v50, v51
	v_log_f32_e32 v50, v50
	v_cvt_pk_f16_f32 v40, v18, v19
	v_cvt_pk_f16_f32 v41, v20, v21
	v_cvt_pk_f16_f32 v42, v22, v23
	v_cvt_pk_f16_f32 v43, v24, v25
	v_cvt_pk_f16_f32 v44, v26, v27
	v_cvt_pk_f16_f32 v45, v28, v29
	v_cvt_pk_f16_f32 v46, v30, v31
	v_cvt_pk_f16_f32 v47, v32, v33
	v_add_f32_e32 v50, 0x41600000, v50
	v_mul_f32_e32 v50, 0xbf317218, v50
	v_cndmask_b32_e64 v51, v50, 1.0, vcc
	s_waitcnt vmcnt(0)
	ds_read_b128 v[2:5], v39
	ds_read_b128 v[6:9], v81
	ds_read_b128 v[10:13], v82
	ds_read_b128 v[14:17], v83
	s_waitcnt lgkmcnt(2)
	v_max3_f32 v52, v2, v3, v4
	v_max3_f32 v53, v5, v6, v7
	v_max_f32_e32 v52, v52, v8
	v_max_f32_e32 v53, v53, v9
	s_waitcnt lgkmcnt(0)
	v_max3_f32 v52, v52, v10, v11
	v_max3_f32 v53, v53, v12, v13
	v_max3_f32 v52, v52, v14, v15
	v_max3_f32 v53, v53, v16, v17
	v_max_f32_e32 v52, v52, v53
	v_mov_b32_e32 v53, v52
	s_nop 1
	v_permlane32_swap_b32_e32 v52, v53
	v_max_f32_e32 v52, v52, v53
	v_cndmask_b32_e32 v54, 1.0, v52, vcc
	v_fmamk_f32 v48, v52, 0x3fb8aa3b, v34
	v_pk_fma_f32 v[2:3], v[2:3], v[84:85], v[48:49] op_sel_hi:[1,0,0] neg_lo:[0,0,1] neg_hi:[0,0,1]
	v_mfma_f32_32x32x2_f32 v[64:79], v54, v51, 0
	v_exp_f32_e32 v2, v2
	v_exp_f32_e32 v3, v3
	v_pk_fma_f32 v[4:5], v[4:5], v[84:85], v[48:49] op_sel_hi:[1,0,0] neg_lo:[0,0,1] neg_hi:[0,0,1]
	v_exp_f32_e32 v4, v4
	v_exp_f32_e32 v5, v5
	v_pk_fma_f32 v[6:7], v[6:7], v[84:85], v[48:49] op_sel_hi:[1,0,0] neg_lo:[0,0,1] neg_hi:[0,0,1]
	v_exp_f32_e32 v6, v6
	v_exp_f32_e32 v7, v7
	v_pk_fma_f32 v[8:9], v[8:9], v[84:85], v[48:49] op_sel_hi:[1,0,0] neg_lo:[0,0,1] neg_hi:[0,0,1]
	v_exp_f32_e32 v8, v8
	v_exp_f32_e32 v9, v9
	v_pk_fma_f32 v[10:11], v[10:11], v[84:85], v[48:49] op_sel_hi:[1,0,0] neg_lo:[0,0,1] neg_hi:[0,0,1]
	v_exp_f32_e32 v10, v10
	v_cvt_pk_f16_f32 v56, v2, v3
	v_cvt_pk_f16_f32 v57, v4, v5
	v_cvt_pk_f16_f32 v58, v6, v7
	v_cvt_pk_f16_f32 v59, v8, v9
	v_exp_f32_e32 v11, v11
	v_pk_fma_f32 v[12:13], v[12:13], v[84:85], v[48:49] op_sel_hi:[1,0,0] neg_lo:[0,0,1] neg_hi:[0,0,1]
	v_exp_f32_e32 v12, v12
	v_mfma_f32_32x32x16_f16 v[18:33], v[56:59], v[40:43], 0
	v_exp_f32_e32 v13, v13
	v_pk_fma_f32 v[14:15], v[14:15], v[84:85], v[48:49] op_sel_hi:[1,0,0] neg_lo:[0,0,1] neg_hi:[0,0,1]
	v_exp_f32_e32 v14, v14
	v_exp_f32_e32 v15, v15
	v_pk_fma_f32 v[16:17], v[16:17], v[84:85], v[48:49] op_sel_hi:[1,0,0] neg_lo:[0,0,1] neg_hi:[0,0,1]
	v_exp_f32_e32 v16, v16
	v_exp_f32_e32 v17, v17
	v_cvt_pk_f16_f32 v60, v10, v11
	v_cvt_pk_f16_f32 v61, v12, v13
	v_cvt_pk_f16_f32 v62, v14, v15
	v_cvt_pk_f16_f32 v63, v16, v17
	s_nop 1
	v_mfma_f32_32x32x16_f16 v[18:33], v[60:63], v[44:47], v[18:33]
	s_nop 11
	v_log_f32_e32 v18, v18
	v_log_f32_e32 v19, v19
	v_log_f32_e32 v20, v20
	v_log_f32_e32 v21, v21
	v_log_f32_e32 v22, v22
	v_log_f32_e32 v23, v23
	v_pk_fma_f32 v[64:65], v[18:19], v[84:85], v[64:65] op_sel:[0,1,0] op_sel_hi:[1,1,1]
	buffer_store_dword v64, v36, s[8:11], 0 offen
	buffer_store_dword v65, v36, s[8:11], s24 offen
	v_log_f32_e32 v24, v24
	v_log_f32_e32 v25, v25
	v_pk_fma_f32 v[66:67], v[20:21], v[84:85], v[66:67] op_sel:[0,1,0] op_sel_hi:[1,1,1]
	buffer_store_dword v66, v36, s[8:11], s25 offen
	buffer_store_dword v67, v36, s[8:11], s26 offen
	v_log_f32_e32 v26, v26
	v_log_f32_e32 v27, v27
	v_pk_fma_f32 v[68:69], v[22:23], v[84:85], v[68:69] op_sel:[0,1,0] op_sel_hi:[1,1,1]
	buffer_store_dword v68, v36, s[8:11], s27 offen
	buffer_store_dword v69, v36, s[8:11], s28 offen
	v_log_f32_e32 v28, v28
	v_log_f32_e32 v29, v29
	v_pk_fma_f32 v[70:71], v[24:25], v[84:85], v[70:71] op_sel:[0,1,0] op_sel_hi:[1,1,1]
	buffer_store_dword v70, v36, s[8:11], s29 offen
	buffer_store_dword v71, v36, s[8:11], s30 offen
	v_log_f32_e32 v30, v30
	v_log_f32_e32 v31, v31
	v_pk_fma_f32 v[72:73], v[26:27], v[84:85], v[72:73] op_sel:[0,1,0] op_sel_hi:[1,1,1]
	buffer_store_dword v72, v36, s[8:11], s31 offen
	buffer_store_dword v73, v36, s[8:11], s32 offen
	v_log_f32_e32 v32, v32
	v_log_f32_e32 v33, v33
	v_pk_fma_f32 v[74:75], v[28:29], v[84:85], v[74:75] op_sel:[0,1,0] op_sel_hi:[1,1,1]
	buffer_store_dword v74, v36, s[8:11], s33 offen
	buffer_store_dword v75, v36, s[8:11], s34 offen
	v_pk_fma_f32 v[76:77], v[30:31], v[84:85], v[76:77] op_sel:[0,1,0] op_sel_hi:[1,1,1]
	buffer_store_dword v76, v36, s[8:11], s35 offen
	buffer_store_dword v77, v36, s[8:11], s36 offen
	v_pk_fma_f32 v[78:79], v[32:33], v[84:85], v[78:79] op_sel:[0,1,0] op_sel_hi:[1,1,1]
	buffer_store_dword v78, v36, s[8:11], s37 offen
	buffer_store_dword v79, v36, s[8:11], s38 offen
	s_endpgm

	.amdhsa_kernel _Z16sum_layer_kernelPKfS0_Pf
		.amdhsa_group_segment_fixed_size 32768
		.amdhsa_private_segment_fixed_size 0
		.amdhsa_kernarg_size 24
		.amdhsa_user_sgpr_count 2
		.amdhsa_user_sgpr_dispatch_ptr 0
		.amdhsa_user_sgpr_queue_ptr 0
		.amdhsa_user_sgpr_kernarg_segment_ptr 1
		.amdhsa_user_sgpr_dispatch_id 0
		.amdhsa_user_sgpr_kernarg_preload_length 0
		.amdhsa_user_sgpr_kernarg_preload_offset 0
		.amdhsa_user_sgpr_private_segment_size 0
		.amdhsa_uses_dynamic_stack 0
		.amdhsa_enable_private_segment 0
		.amdhsa_system_sgpr_workgroup_id_x 1
		.amdhsa_system_sgpr_workgroup_id_y 0
		.amdhsa_system_sgpr_workgroup_id_z 0
		.amdhsa_system_sgpr_workgroup_info 0
		.amdhsa_system_vgpr_workitem_id 0
		.amdhsa_next_free_vgpr 88
		.amdhsa_next_free_sgpr 55
		.amdhsa_accum_offset 88
		.amdhsa_reserve_vcc 1
		.amdhsa_float_round_mode_32 0
		.amdhsa_float_round_mode_16_64 0
		.amdhsa_float_denorm_mode_32 3
		.amdhsa_float_denorm_mode_16_64 3
		.amdhsa_dx10_clamp 1
		.amdhsa_ieee_mode 1
		.amdhsa_fp16_overflow 0
		.amdhsa_tg_split 0
		.amdhsa_exception_fp_ieee_invalid_op 0
		.amdhsa_exception_fp_denorm_src 0
		.amdhsa_exception_fp_ieee_div_zero 0
		.amdhsa_exception_fp_ieee_overflow 0
		.amdhsa_exception_fp_ieee_underflow 0
		.amdhsa_exception_fp_ieee_inexact 0
		.amdhsa_exception_int_div_zero 0
	.end_amdhsa_kernel

amdhsa.kernels:
  - .agpr_count:     0
    .args:
      - .address_space:  global
        .offset:         0
        .size:           8
        .value_kind:     global_buffer
      - .address_space:  global
        .offset:         8
        .size:           8
        .value_kind:     global_buffer
      - .address_space:  global
        .offset:         16
        .size:           8
        .value_kind:     global_buffer
    .group_segment_fixed_size: 32768
    .kernarg_segment_align: 8
    .kernarg_segment_size: 24
    .language:       OpenCL C
    .language_version:
      - 2
      - 0
    .max_flat_workgroup_size: 256
    .name:           _Z16sum_layer_kernelPKfS0_Pf
    .private_segment_fixed_size: 0
    .sgpr_count:     61
    .sgpr_spill_count: 0
    .symbol:         _Z16sum_layer_kernelPKfS0_Pf.kd
    .uniform_work_group_size: 1
    .uses_dynamic_stack: false
    .vgpr_count:     88
    .vgpr_spill_count: 0
    .wavefront_size: 64
